# combo4 + P2 epilogue QK-norm sums: permlane32/16 swap pair-reductions + one full-wave ds_write per 4 values instead of 32 serial ds_bpermute; gain loads hoisted above the barrier
# baseline (speedup 1.0000x reference)
.LBB0_212:
	s_cmp_lg_u64 s[44:45], 0
	v_pk_mul_f32 v[158:159], v[158:159], s[26:27] op_sel_hi:[1,0]
	v_pk_mul_f32 v[156:157], v[156:157], s[26:27] op_sel_hi:[1,0]
	v_pk_mul_f32 v[154:155], v[154:155], s[26:27] op_sel_hi:[1,0]
	v_pk_mul_f32 v[152:153], v[152:153], s[26:27] op_sel_hi:[1,0]
	v_pk_mul_f32 v[150:151], v[150:151], s[26:27] op_sel_hi:[1,0]
	v_pk_mul_f32 v[148:149], v[148:149], s[26:27] op_sel_hi:[1,0]
	v_pk_mul_f32 v[146:147], v[146:147], s[26:27] op_sel_hi:[1,0]
	v_pk_mul_f32 v[144:145], v[144:145], s[26:27] op_sel_hi:[1,0]
	v_pk_mul_f32 v[142:143], v[142:143], s[26:27] op_sel_hi:[1,0]
	v_pk_mul_f32 v[140:141], v[140:141], s[26:27] op_sel_hi:[1,0]
	v_pk_mul_f32 v[138:139], v[138:139], s[26:27] op_sel_hi:[1,0]
	v_pk_mul_f32 v[136:137], v[136:137], s[26:27] op_sel_hi:[1,0]
	v_pk_mul_f32 v[134:135], v[134:135], s[26:27] op_sel_hi:[1,0]
	v_pk_mul_f32 v[132:133], v[132:133], s[26:27] op_sel_hi:[1,0]
	v_pk_mul_f32 v[130:131], v[130:131], s[26:27] op_sel_hi:[1,0]
	v_pk_mul_f32 v[128:129], v[128:129], s[26:27] op_sel_hi:[1,0]
	v_pk_mul_f32 v[126:127], v[126:127], s[26:27] op_sel_hi:[1,0]
	v_pk_mul_f32 v[178:179], v[124:125], s[26:27] op_sel_hi:[1,0]
	v_pk_mul_f32 v[124:125], v[122:123], s[26:27] op_sel_hi:[1,0]
	v_pk_mul_f32 v[180:181], v[120:121], s[26:27] op_sel_hi:[1,0]
	v_pk_mul_f32 v[118:119], v[118:119], s[26:27] op_sel_hi:[1,0]
	v_pk_mul_f32 v[120:121], v[116:117], s[26:27] op_sel_hi:[1,0]
	v_pk_mul_f32 v[116:117], v[114:115], s[26:27] op_sel_hi:[1,0]
	v_pk_mul_f32 v[122:123], v[112:113], s[26:27] op_sel_hi:[1,0]
	v_pk_mul_f32 v[110:111], v[110:111], s[26:27] op_sel_hi:[1,0]
	v_pk_mul_f32 v[108:109], v[108:109], s[26:27] op_sel_hi:[1,0]
	v_pk_mul_f32 v[106:107], v[106:107], s[26:27] op_sel_hi:[1,0]
	v_pk_mul_f32 v[112:113], v[104:105], s[26:27] op_sel_hi:[1,0]
	v_pk_mul_f32 v[102:103], v[102:103], s[26:27] op_sel_hi:[1,0]
	v_pk_mul_f32 v[100:101], v[100:101], s[26:27] op_sel_hi:[1,0]
	v_pk_mul_f32 v[98:99], v[98:99], s[26:27] op_sel_hi:[1,0]
	v_pk_mul_f32 v[96:97], v[96:97], s[26:27] op_sel_hi:[1,0]
	v_pk_mul_f32 v[94:95], v[94:95], s[26:27] op_sel_hi:[1,0]
	v_pk_mul_f32 v[92:93], v[92:93], s[26:27] op_sel_hi:[1,0]
	v_pk_mul_f32 v[90:91], v[90:91], s[26:27] op_sel_hi:[1,0]
	v_pk_mul_f32 v[88:89], v[88:89], s[26:27] op_sel_hi:[1,0]
	v_pk_mul_f32 v[86:87], v[86:87], s[26:27] op_sel_hi:[1,0]
	v_pk_mul_f32 v[84:85], v[84:85], s[26:27] op_sel_hi:[1,0]
	v_pk_mul_f32 v[82:83], v[82:83], s[26:27] op_sel_hi:[1,0]
	v_pk_mul_f32 v[80:81], v[80:81], s[26:27] op_sel_hi:[1,0]
	v_pk_mul_f32 v[78:79], v[78:79], s[26:27] op_sel_hi:[1,0]
	v_pk_mul_f32 v[76:77], v[76:77], s[26:27] op_sel_hi:[1,0]
	v_pk_mul_f32 v[74:75], v[74:75], s[26:27] op_sel_hi:[1,0]
	v_pk_mul_f32 v[72:73], v[72:73], s[26:27] op_sel_hi:[1,0]
	v_pk_mul_f32 v[70:71], v[70:71], s[26:27] op_sel_hi:[1,0]
	v_pk_mul_f32 v[68:69], v[68:69], s[26:27] op_sel_hi:[1,0]
	v_pk_mul_f32 v[66:67], v[66:67], s[26:27] op_sel_hi:[1,0]
	v_pk_mul_f32 v[64:65], v[64:65], s[26:27] op_sel_hi:[1,0]
	v_pk_mul_f32 v[62:63], v[62:63], s[26:27] op_sel_hi:[1,0]
	v_pk_mul_f32 v[104:105], v[60:61], s[26:27] op_sel_hi:[1,0]
	v_pk_mul_f32 v[60:61], v[58:59], s[26:27] op_sel_hi:[1,0]
	v_pk_mul_f32 v[114:115], v[56:57], s[26:27] op_sel_hi:[1,0]
	v_pk_mul_f32 v[54:55], v[54:55], s[26:27] op_sel_hi:[1,0]
	v_pk_mul_f32 v[56:57], v[52:53], s[26:27] op_sel_hi:[1,0]
	v_pk_mul_f32 v[52:53], v[50:51], s[26:27] op_sel_hi:[1,0]
	v_pk_mul_f32 v[58:59], v[48:49], s[26:27] op_sel_hi:[1,0]
	v_pk_mul_f32 v[46:47], v[46:47], s[26:27] op_sel_hi:[1,0]
	v_pk_mul_f32 v[48:49], v[44:45], s[26:27] op_sel_hi:[1,0]
	v_pk_mul_f32 v[44:45], v[42:43], s[26:27] op_sel_hi:[1,0]
	v_pk_mul_f32 v[50:51], v[40:41], s[26:27] op_sel_hi:[1,0]
	v_pk_mul_f32 v[38:39], v[38:39], s[26:27] op_sel_hi:[1,0]
	v_pk_mul_f32 v[40:41], v[36:37], s[26:27] op_sel_hi:[1,0]
	v_pk_mul_f32 v[36:37], v[34:35], s[26:27] op_sel_hi:[1,0]
	s_cselect_b64 s[42:43], -1, 0
	s_cmp_eq_u64 s[44:45], 0
	v_pk_mul_f32 v[42:43], v[32:33], s[26:27] op_sel_hi:[1,0]
	v_readlane_b32 s68, v254, 16
	v_readlane_b32 s69, v254, 17
	s_cbranch_scc1 .LBB0_246
	s_lshl_b32 s29, s54, 2
	s_add_u32 s44, s44, s29
	s_addc_u32 s45, s45, 0
	v_lshlrev_b32_e32 v0, 2, v170
	global_load_dwordx4 v[4:7], v0, s[44:45]
	global_load_dwordx4 v[0:3], v0, s[44:45] offset:16
	v_mul_f32_e32 v222, v157, v157
	v_mul_f32_e32 v238, v159, v159
	v_fmac_f32_e32 v222, v156, v156
	v_fmac_f32_e32 v238, v158, v158
	v_add_f32_e32 v222, v222, v238
	v_mul_f32_e32 v238, v153, v153
	v_fmac_f32_e32 v238, v152, v152
	v_add_f32_e32 v222, v222, v238
	v_mul_f32_e32 v238, v155, v155
	v_fmac_f32_e32 v238, v154, v154
	v_add_f32_e32 v222, v238, v222
	v_mul_f32_e32 v223, v179, v179
	v_mul_f32_e32 v239, v127, v127
	v_fmac_f32_e32 v223, v178, v178
	v_fmac_f32_e32 v239, v126, v126
	v_add_f32_e32 v223, v223, v239
	v_mul_f32_e32 v239, v181, v181
	v_fmac_f32_e32 v239, v180, v180
	v_add_f32_e32 v223, v223, v239
	v_mul_f32_e32 v239, v125, v125
	v_fmac_f32_e32 v239, v124, v124
	v_add_f32_e32 v223, v239, v223
	v_mul_f32_e32 v224, v149, v149
	v_mul_f32_e32 v240, v151, v151
	v_fmac_f32_e32 v224, v148, v148
	v_fmac_f32_e32 v240, v150, v150
	v_add_f32_e32 v224, v224, v240
	v_mul_f32_e32 v240, v145, v145
	v_fmac_f32_e32 v240, v144, v144
	v_add_f32_e32 v224, v224, v240
	v_mul_f32_e32 v240, v147, v147
	v_fmac_f32_e32 v240, v146, v146
	v_add_f32_e32 v224, v240, v224
	v_mul_f32_e32 v225, v121, v121
	v_mul_f32_e32 v241, v119, v119
	v_fmac_f32_e32 v225, v120, v120
	v_fmac_f32_e32 v241, v118, v118
	v_add_f32_e32 v225, v225, v241
	v_mul_f32_e32 v241, v123, v123
	v_fmac_f32_e32 v241, v122, v122
	v_add_f32_e32 v225, v225, v241
	v_mul_f32_e32 v241, v117, v117
	v_fmac_f32_e32 v241, v116, v116
	v_add_f32_e32 v225, v241, v225
	v_mul_f32_e32 v226, v141, v141
	v_mul_f32_e32 v242, v143, v143
	v_fmac_f32_e32 v226, v140, v140
	v_fmac_f32_e32 v242, v142, v142
	v_add_f32_e32 v226, v226, v242
	v_mul_f32_e32 v242, v137, v137
	v_fmac_f32_e32 v242, v136, v136
	v_add_f32_e32 v226, v226, v242
	v_mul_f32_e32 v242, v139, v139
	v_fmac_f32_e32 v242, v138, v138
	v_add_f32_e32 v226, v242, v226
	v_mul_f32_e32 v227, v109, v109
	v_mul_f32_e32 v243, v111, v111
	v_fmac_f32_e32 v227, v108, v108
	v_fmac_f32_e32 v243, v110, v110
	v_add_f32_e32 v227, v227, v243
	v_mul_f32_e32 v243, v113, v113
	v_fmac_f32_e32 v243, v112, v112
	v_add_f32_e32 v227, v227, v243
	v_mul_f32_e32 v243, v107, v107
	v_fmac_f32_e32 v243, v106, v106
	v_add_f32_e32 v227, v243, v227
	v_mul_f32_e32 v228, v133, v133
	v_mul_f32_e32 v244, v135, v135
	v_fmac_f32_e32 v228, v132, v132
	v_fmac_f32_e32 v244, v134, v134
	v_add_f32_e32 v228, v228, v244
	v_mul_f32_e32 v244, v129, v129
	v_fmac_f32_e32 v244, v128, v128
	v_add_f32_e32 v228, v228, v244
	v_mul_f32_e32 v244, v131, v131
	v_fmac_f32_e32 v244, v130, v130
	v_add_f32_e32 v228, v244, v228
	v_mul_f32_e32 v229, v101, v101
	v_mul_f32_e32 v245, v103, v103
	v_fmac_f32_e32 v229, v100, v100
	v_fmac_f32_e32 v245, v102, v102
	v_add_f32_e32 v229, v229, v245
	v_mul_f32_e32 v245, v97, v97
	v_fmac_f32_e32 v245, v96, v96
	v_add_f32_e32 v229, v229, v245
	v_mul_f32_e32 v245, v99, v99
	v_fmac_f32_e32 v245, v98, v98
	v_add_f32_e32 v229, v245, v229
	v_mul_f32_e32 v230, v93, v93
	v_mul_f32_e32 v246, v95, v95
	v_fmac_f32_e32 v230, v92, v92
	v_fmac_f32_e32 v246, v94, v94
	v_add_f32_e32 v230, v230, v246
	v_mul_f32_e32 v246, v89, v89
	v_fmac_f32_e32 v246, v88, v88
	v_add_f32_e32 v230, v230, v246
	v_mul_f32_e32 v246, v91, v91
	v_fmac_f32_e32 v246, v90, v90
	v_add_f32_e32 v230, v246, v230
	v_mul_f32_e32 v231, v105, v105
	v_mul_f32_e32 v247, v63, v63
	v_fmac_f32_e32 v231, v104, v104
	v_fmac_f32_e32 v247, v62, v62
	v_add_f32_e32 v231, v231, v247
	v_mul_f32_e32 v247, v115, v115
	v_fmac_f32_e32 v247, v114, v114
	v_add_f32_e32 v231, v231, v247
	v_mul_f32_e32 v247, v61, v61
	v_fmac_f32_e32 v247, v60, v60
	v_add_f32_e32 v231, v247, v231
	v_mul_f32_e32 v232, v85, v85
	v_mul_f32_e32 v248, v87, v87
	v_fmac_f32_e32 v232, v84, v84
	v_fmac_f32_e32 v248, v86, v86
	v_add_f32_e32 v232, v232, v248
	v_mul_f32_e32 v248, v81, v81
	v_fmac_f32_e32 v248, v80, v80
	v_add_f32_e32 v232, v232, v248
	v_mul_f32_e32 v248, v83, v83
	v_fmac_f32_e32 v248, v82, v82
	v_add_f32_e32 v232, v248, v232
	v_mul_f32_e32 v233, v57, v57
	v_mul_f32_e32 v249, v55, v55
	v_fmac_f32_e32 v233, v56, v56
	v_fmac_f32_e32 v249, v54, v54
	v_add_f32_e32 v233, v233, v249
	v_mul_f32_e32 v249, v59, v59
	v_fmac_f32_e32 v249, v58, v58
	v_add_f32_e32 v233, v233, v249
	v_mul_f32_e32 v249, v53, v53
	v_fmac_f32_e32 v249, v52, v52
	v_add_f32_e32 v233, v249, v233
	v_mul_f32_e32 v234, v77, v77
	v_mul_f32_e32 v250, v79, v79
	v_fmac_f32_e32 v234, v76, v76
	v_fmac_f32_e32 v250, v78, v78
	v_add_f32_e32 v234, v234, v250
	v_mul_f32_e32 v250, v73, v73
	v_fmac_f32_e32 v250, v72, v72
	v_add_f32_e32 v234, v234, v250
	v_mul_f32_e32 v250, v75, v75
	v_fmac_f32_e32 v250, v74, v74
	v_add_f32_e32 v234, v250, v234
	v_mul_f32_e32 v235, v49, v49
	v_mul_f32_e32 v251, v47, v47
	v_fmac_f32_e32 v235, v48, v48
	v_fmac_f32_e32 v251, v46, v46
	v_add_f32_e32 v235, v235, v251
	v_mul_f32_e32 v251, v51, v51
	v_fmac_f32_e32 v251, v50, v50
	v_add_f32_e32 v235, v235, v251
	v_mul_f32_e32 v251, v45, v45
	v_fmac_f32_e32 v251, v44, v44
	v_add_f32_e32 v235, v251, v235
	v_mul_f32_e32 v236, v69, v69
	v_mul_f32_e32 v252, v71, v71
	v_fmac_f32_e32 v236, v68, v68
	v_fmac_f32_e32 v252, v70, v70
	v_add_f32_e32 v236, v236, v252
	v_mul_f32_e32 v252, v65, v65
	v_fmac_f32_e32 v252, v64, v64
	v_add_f32_e32 v236, v236, v252
	v_mul_f32_e32 v252, v67, v67
	v_fmac_f32_e32 v252, v66, v66
	v_add_f32_e32 v236, v252, v236
	v_mul_f32_e32 v237, v41, v41
	v_mul_f32_e32 v253, v39, v39
	v_fmac_f32_e32 v237, v40, v40
	v_fmac_f32_e32 v253, v38, v38
	v_add_f32_e32 v237, v237, v253
	v_mul_f32_e32 v253, v43, v43
	v_fmac_f32_e32 v253, v42, v42
	v_add_f32_e32 v237, v237, v253
	v_mul_f32_e32 v253, v37, v37
	v_fmac_f32_e32 v253, v36, v36
	v_add_f32_e32 v237, v253, v237
	v_lshrrev_b32_e32 v253, 3, v170
	v_and_b32_e32 v252, 1, v253
	v_lshrrev_b32_e32 v253, 1, v253
	v_lshlrev_b32_e32 v253, 4, v253
	v_lshl_add_u32 v253, v252, 9, v253
	v_add_u32_e32 v253, v253, v203
	s_nop 1
	v_permlane32_swap_b32_e32 v222, v223
	v_permlane32_swap_b32_e32 v224, v225
	s_nop 1
	v_add_f32_e32 v222, v222, v223
	v_add_f32_e32 v224, v224, v225
	s_nop 1
	v_permlane16_swap_b32_e32 v222, v224
	s_nop 1
	v_add_f32_e32 v222, v222, v224
	ds_write_b32 v253, v222
	v_permlane32_swap_b32_e32 v226, v227
	v_permlane32_swap_b32_e32 v228, v229
	s_nop 1
	v_add_f32_e32 v226, v226, v227
	v_add_f32_e32 v228, v228, v229
	s_nop 1
	v_permlane16_swap_b32_e32 v226, v228
	s_nop 1
	v_add_f32_e32 v226, v226, v228
	ds_write_b32 v253, v226 offset:1024
	v_permlane32_swap_b32_e32 v230, v231
	v_permlane32_swap_b32_e32 v232, v233
	s_nop 1
	v_add_f32_e32 v230, v230, v231
	v_add_f32_e32 v232, v232, v233
	s_nop 1
	v_permlane16_swap_b32_e32 v230, v232
	s_nop 1
	v_add_f32_e32 v230, v230, v232
	ds_write_b32 v253, v230 offset:4096
	v_permlane32_swap_b32_e32 v234, v235
	v_permlane32_swap_b32_e32 v236, v237
	s_nop 1
	v_add_f32_e32 v234, v234, v235
	v_add_f32_e32 v236, v236, v237
	s_nop 1
	v_permlane16_swap_b32_e32 v234, v236
	s_nop 1
	v_add_f32_e32 v234, v234, v236
	ds_write_b32 v253, v234 offset:5120
	s_mov_b64 s[46:47], exec
	s_waitcnt lgkmcnt(0)
	s_barrier
	s_waitcnt lgkmcnt(0)
	ds_read_b128 v[8:11], v202
	ds_read_b128 v[12:15], v202 offset:16
	ds_read_b128 v[16:19], v202 offset:528
	ds_read_b128 v[20:23], v202 offset:1040
	ds_read_b128 v[28:31], v206
	ds_read_b128 v[24:27], v208
	ds_read_b128 v[32:35], v204
	ds_read_b128 v[182:185], v202 offset:5648
	s_waitcnt lgkmcnt(0)
	v_mov_b32_e32 v176, v9
	v_mov_b32_e32 v177, v10
	v_mov_b32_e32 v9, v11
	v_mov_b32_e32 v10, v13
	v_mov_b32_e32 v11, v14
	v_mov_b32_e32 v13, v15
	v_mov_b32_e32 v14, v33
	v_mov_b32_e32 v15, v34
	v_mov_b32_e32 v33, v35
	v_mov_b32_e32 v34, v17
	v_mov_b32_e32 v35, v18
	v_mov_b32_e32 v17, v19
	v_mov_b32_e32 v18, v29
	v_mov_b32_e32 v19, v30
	v_mov_b32_e32 v29, v31
	v_pk_add_f32 v[8:9], v[176:177], v[8:9]
	v_pk_add_f32 v[10:11], v[10:11], v[12:13]
	v_pk_add_f32 v[12:13], v[14:15], v[32:33]
	v_pk_add_f32 v[14:15], v[34:35], v[16:17]
	v_pk_add_f32 v[16:17], v[18:19], v[28:29]
	v_add_f32_e32 v8, v8, v9
	v_add_f32_e32 v9, v10, v11
	v_add_f32_e32 v10, v12, v13
	v_add_f32_e32 v12, v16, v17
	v_fmamk_f32 v9, v9, 0x3c000000, v219
	v_add_f32_e32 v11, v14, v15
	v_fmamk_f32 v13, v10, 0x3c000000, v219
	v_fmamk_f32 v15, v12, 0x3c000000, v219
	v_rsq_f32_e32 v10, v9
	v_rsq_f32_e32 v16, v15
	v_fmamk_f32 v11, v11, 0x3c000000, v219
	v_rsq_f32_e32 v14, v11
	v_pk_mul_f32 v[32:33], v[178:179], v[10:11] op_sel_hi:[1,0]
	v_pk_mul_f32 v[34:35], v[126:127], v[10:11] op_sel_hi:[1,0]
	v_pk_mul_f32 v[176:177], v[180:181], v[10:11] op_sel_hi:[1,0]
	v_pk_mul_f32 v[10:11], v[124:125], v[10:11] op_sel_hi:[1,0]
	v_fmamk_f32 v8, v8, 0x3c000000, v219
	v_rsq_f32_e32 v12, v13
	v_rsq_f32_e32 v8, v8
	v_pk_mul_f32 v[120:121], v[120:121], v[14:15] op_sel_hi:[1,0]
	v_pk_mul_f32 v[118:119], v[118:119], v[14:15] op_sel_hi:[1,0]
	v_pk_mul_f32 v[148:149], v[148:149], v[12:13] op_sel_hi:[1,0]
	v_pk_mul_f32 v[150:151], v[150:151], v[12:13] op_sel_hi:[1,0]
	v_pk_mul_f32 v[144:145], v[144:145], v[12:13] op_sel_hi:[1,0]
	v_pk_mul_f32 v[12:13], v[146:147], v[12:13] op_sel_hi:[1,0]
	v_pk_mul_f32 v[18:19], v[156:157], v[8:9] op_sel_hi:[1,0]
	v_pk_mul_f32 v[28:29], v[158:159], v[8:9] op_sel_hi:[1,0]
	v_pk_mul_f32 v[30:31], v[152:153], v[8:9] op_sel_hi:[1,0]
	v_pk_mul_f32 v[8:9], v[154:155], v[8:9] op_sel_hi:[1,0]
	v_pk_mul_f32 v[122:123], v[122:123], v[14:15] op_sel_hi:[1,0]
	v_pk_mul_f32 v[14:15], v[116:117], v[14:15] op_sel_hi:[1,0]
	s_waitcnt vmcnt(0)
	v_pk_mul_f32 v[156:157], v[4:5], v[18:19]
	v_pk_mul_f32 v[124:125], v[2:3], v[10:11]
	v_pk_mul_f32 v[10:11], v[142:143], v[16:17] op_sel_hi:[1,0]
	v_pk_mul_f32 v[146:147], v[2:3], v[12:13]
	v_pk_mul_f32 v[142:143], v[6:7], v[10:11]
	v_mov_b32_e32 v10, v21
	v_mov_b32_e32 v11, v22
	v_mov_b32_e32 v21, v23
	v_pk_add_f32 v[10:11], v[10:11], v[20:21]
	v_pk_mul_f32 v[12:13], v[138:139], v[16:17] op_sel_hi:[1,0]
	v_add_f32_e32 v10, v10, v11
	v_fmamk_f32 v10, v10, 0x3c000000, v219
	v_rsq_f32_e32 v10, v10
	v_pk_mul_f32 v[154:155], v[2:3], v[8:9]
	v_pk_mul_f32 v[8:9], v[140:141], v[16:17] op_sel_hi:[1,0]
	v_pk_mul_f32 v[138:139], v[2:3], v[12:13]
	v_pk_mul_f32 v[12:13], v[110:111], v[10:11] op_sel_hi:[1,0]
	v_pk_mul_f32 v[140:141], v[4:5], v[8:9]
	v_pk_mul_f32 v[8:9], v[136:137], v[16:17] op_sel_hi:[1,0]
	v_pk_mul_f32 v[110:111], v[6:7], v[12:13]
	v_mov_b32_e32 v12, v25
	v_mov_b32_e32 v13, v26
	v_mov_b32_e32 v25, v27
	v_pk_mul_f32 v[136:137], v[0:1], v[8:9]
	v_pk_mul_f32 v[8:9], v[108:109], v[10:11] op_sel_hi:[1,0]
	v_pk_add_f32 v[12:13], v[12:13], v[24:25]
	v_pk_mul_f32 v[108:109], v[4:5], v[8:9]
	v_pk_mul_f32 v[8:9], v[112:113], v[10:11] op_sel_hi:[1,0]
	v_add_f32_e32 v11, v12, v13
	v_fmamk_f32 v11, v11, 0x3c000000, v219
	v_rsq_f32_e32 v16, v11
	v_pk_mul_f32 v[10:11], v[106:107], v[10:11] op_sel_hi:[1,0]
	v_pk_mul_f32 v[112:113], v[0:1], v[8:9]
	v_pk_mul_f32 v[106:107], v[2:3], v[10:11]
	ds_read_b128 v[8:11], v202 offset:1552
	v_pk_mul_f32 v[116:117], v[2:3], v[14:15]
	v_pk_mul_f32 v[12:13], v[132:133], v[16:17] op_sel_hi:[1,0]
	v_pk_mul_f32 v[14:15], v[134:135], v[16:17] op_sel_hi:[1,0]
	v_pk_mul_f32 v[132:133], v[4:5], v[12:13]
	v_pk_mul_f32 v[134:135], v[6:7], v[14:15]
	ds_read_b128 v[12:15], v202 offset:4112
	s_waitcnt lgkmcnt(1)
	v_mov_b32_e32 v20, v9
	v_mov_b32_e32 v21, v10
	v_mov_b32_e32 v9, v11
	v_pk_add_f32 v[8:9], v[20:21], v[8:9]
	v_pk_mul_f32 v[18:19], v[128:129], v[16:17] op_sel_hi:[1,0]
	v_add_f32_e32 v8, v8, v9
	v_fmamk_f32 v8, v8, 0x3c000000, v219
	v_rsq_f32_e32 v20, v8
	v_pk_mul_f32 v[8:9], v[130:131], v[16:17] op_sel_hi:[1,0]
	v_pk_mul_f32 v[128:129], v[0:1], v[18:19]
	v_pk_mul_f32 v[130:131], v[2:3], v[8:9]
	ds_read_b128 v[8:11], v210
	v_pk_mul_f32 v[16:17], v[100:101], v[20:21] op_sel_hi:[1,0]
	v_pk_mul_f32 v[18:19], v[102:103], v[20:21] op_sel_hi:[1,0]
	v_pk_mul_f32 v[100:101], v[4:5], v[16:17]
	v_pk_mul_f32 v[102:103], v[6:7], v[18:19]
	ds_read_b128 v[16:19], v212
	s_waitcnt lgkmcnt(1)
	v_mov_b32_e32 v24, v9
	v_mov_b32_e32 v25, v10
	v_mov_b32_e32 v9, v11
	v_pk_add_f32 v[8:9], v[24:25], v[8:9]
	v_pk_mul_f32 v[22:23], v[96:97], v[20:21] op_sel_hi:[1,0]
	v_add_f32_e32 v8, v8, v9
	v_fmamk_f32 v8, v8, 0x3c000000, v219
	v_rsq_f32_e32 v8, v8
	v_pk_mul_f32 v[10:11], v[98:99], v[20:21] op_sel_hi:[1,0]
	v_pk_mul_f32 v[96:97], v[0:1], v[22:23]
	v_pk_mul_f32 v[98:99], v[2:3], v[10:11]
	v_pk_mul_f32 v[20:21], v[94:95], v[8:9] op_sel_hi:[1,0]
	v_pk_mul_f32 v[10:11], v[92:93], v[8:9] op_sel_hi:[1,0]
	v_pk_mul_f32 v[94:95], v[6:7], v[20:21]
	v_mov_b32_e32 v20, v13
	v_mov_b32_e32 v21, v14
	v_mov_b32_e32 v13, v15
	v_pk_add_f32 v[12:13], v[20:21], v[12:13]
	v_pk_mul_f32 v[92:93], v[4:5], v[10:11]
	v_pk_mul_f32 v[10:11], v[88:89], v[8:9] op_sel_hi:[1,0]
	v_add_f32_e32 v9, v12, v13
	v_fmamk_f32 v9, v9, 0x3c000000, v219
	v_rsq_f32_e32 v12, v9
	v_pk_mul_f32 v[88:89], v[0:1], v[10:11]
	v_pk_mul_f32 v[8:9], v[90:91], v[8:9] op_sel_hi:[1,0]
	v_pk_mul_f32 v[158:159], v[6:7], v[28:29]
	v_pk_mul_f32 v[10:11], v[62:63], v[12:13] op_sel_hi:[1,0]
	v_pk_mul_f32 v[90:91], v[2:3], v[8:9]
	v_pk_mul_f32 v[62:63], v[6:7], v[10:11]
	s_waitcnt lgkmcnt(0)
	v_mov_b32_e32 v10, v17
	v_mov_b32_e32 v11, v18
	v_mov_b32_e32 v17, v19
	v_pk_add_f32 v[10:11], v[10:11], v[16:17]
	v_pk_mul_f32 v[8:9], v[104:105], v[12:13] op_sel_hi:[1,0]
	v_add_f32_e32 v10, v10, v11
	v_fmamk_f32 v10, v10, 0x3c000000, v219
	v_pk_mul_f32 v[104:105], v[4:5], v[8:9]
	v_pk_mul_f32 v[8:9], v[114:115], v[12:13] op_sel_hi:[1,0]
	v_rsq_f32_e32 v16, v10
	v_pk_mul_f32 v[10:11], v[60:61], v[12:13] op_sel_hi:[1,0]
	v_pk_mul_f32 v[114:115], v[0:1], v[8:9]
	v_pk_mul_f32 v[60:61], v[2:3], v[10:11]
	ds_read_b128 v[8:11], v202 offset:4624
	v_pk_mul_f32 v[12:13], v[84:85], v[16:17] op_sel_hi:[1,0]
	v_pk_mul_f32 v[14:15], v[86:87], v[16:17] op_sel_hi:[1,0]
	v_pk_mul_f32 v[84:85], v[4:5], v[12:13]
	v_pk_mul_f32 v[86:87], v[6:7], v[14:15]
	ds_read_b128 v[12:15], v202 offset:5136
	s_waitcnt lgkmcnt(1)
	v_mov_b32_e32 v20, v9
	v_mov_b32_e32 v21, v10
	v_mov_b32_e32 v9, v11
	v_pk_add_f32 v[8:9], v[20:21], v[8:9]
	v_pk_mul_f32 v[18:19], v[80:81], v[16:17] op_sel_hi:[1,0]
	v_add_f32_e32 v8, v8, v9
	v_fmamk_f32 v8, v8, 0x3c000000, v219
	v_rsq_f32_e32 v20, v8
	v_pk_mul_f32 v[8:9], v[82:83], v[16:17] op_sel_hi:[1,0]
	v_pk_mul_f32 v[80:81], v[0:1], v[18:19]
	v_pk_mul_f32 v[82:83], v[2:3], v[8:9]
	ds_read_b128 v[8:11], v214
	v_pk_mul_f32 v[16:17], v[56:57], v[20:21] op_sel_hi:[1,0]
	v_pk_mul_f32 v[18:19], v[54:55], v[20:21] op_sel_hi:[1,0]
	v_pk_mul_f32 v[56:57], v[4:5], v[16:17]
	v_pk_mul_f32 v[54:55], v[6:7], v[18:19]
	ds_read_b128 v[16:19], v216
	s_waitcnt lgkmcnt(1)
	v_mov_b32_e32 v24, v9
	v_mov_b32_e32 v25, v10
	v_mov_b32_e32 v9, v11
	v_pk_add_f32 v[8:9], v[24:25], v[8:9]
	v_pk_mul_f32 v[22:23], v[58:59], v[20:21] op_sel_hi:[1,0]
	v_add_f32_e32 v8, v8, v9
	v_fmamk_f32 v8, v8, 0x3c000000, v219
	v_rsq_f32_e32 v8, v8
	v_pk_mul_f32 v[10:11], v[52:53], v[20:21] op_sel_hi:[1,0]
	v_pk_mul_f32 v[126:127], v[6:7], v[34:35]
	v_pk_mul_f32 v[52:53], v[2:3], v[10:11]
	v_pk_mul_f32 v[20:21], v[78:79], v[8:9] op_sel_hi:[1,0]
	v_pk_mul_f32 v[10:11], v[76:77], v[8:9] op_sel_hi:[1,0]
	v_pk_mul_f32 v[78:79], v[6:7], v[20:21]
	v_mov_b32_e32 v20, v13
	v_mov_b32_e32 v21, v14
	v_mov_b32_e32 v13, v15
	v_pk_add_f32 v[12:13], v[20:21], v[12:13]
	v_pk_mul_f32 v[76:77], v[4:5], v[10:11]
	v_pk_mul_f32 v[10:11], v[72:73], v[8:9] op_sel_hi:[1,0]
	v_add_f32_e32 v9, v12, v13
	v_fmamk_f32 v9, v9, 0x3c000000, v219
	v_rsq_f32_e32 v12, v9
	v_pk_mul_f32 v[72:73], v[0:1], v[10:11]
	v_pk_mul_f32 v[8:9], v[74:75], v[8:9] op_sel_hi:[1,0]
	v_pk_mul_f32 v[178:179], v[4:5], v[32:33]
	v_pk_mul_f32 v[10:11], v[46:47], v[12:13] op_sel_hi:[1,0]
	v_pk_mul_f32 v[74:75], v[2:3], v[8:9]
	v_pk_mul_f32 v[46:47], v[6:7], v[10:11]
	s_waitcnt lgkmcnt(0)
	v_mov_b32_e32 v10, v17
	v_mov_b32_e32 v11, v18
	v_mov_b32_e32 v17, v19
	v_pk_add_f32 v[10:11], v[10:11], v[16:17]
	v_pk_mul_f32 v[8:9], v[48:49], v[12:13] op_sel_hi:[1,0]
	v_add_f32_e32 v10, v10, v11
	v_fmamk_f32 v10, v10, 0x3c000000, v219
	v_rsq_f32_e32 v10, v10
	v_pk_mul_f32 v[48:49], v[4:5], v[8:9]
	v_pk_mul_f32 v[8:9], v[50:51], v[12:13] op_sel_hi:[1,0]
	v_pk_mul_f32 v[12:13], v[44:45], v[12:13] op_sel_hi:[1,0]
	v_pk_mul_f32 v[50:51], v[0:1], v[8:9]
	v_pk_mul_f32 v[44:45], v[2:3], v[12:13]
	v_pk_mul_f32 v[12:13], v[70:71], v[10:11] op_sel_hi:[1,0]
	v_pk_mul_f32 v[8:9], v[68:69], v[10:11] op_sel_hi:[1,0]
	v_pk_mul_f32 v[70:71], v[6:7], v[12:13]
	v_mov_b32_e32 v12, v183
	v_mov_b32_e32 v13, v184
	v_mov_b32_e32 v183, v185
	v_pk_add_f32 v[12:13], v[12:13], v[182:183]
	v_pk_mul_f32 v[68:69], v[4:5], v[8:9]
	v_pk_mul_f32 v[8:9], v[64:65], v[10:11] op_sel_hi:[1,0]
	v_add_f32_e32 v11, v12, v13
	v_fmamk_f32 v11, v11, 0x3c000000, v219
	v_rsq_f32_e32 v12, v11
	v_pk_mul_f32 v[10:11], v[66:67], v[10:11] op_sel_hi:[1,0]
	v_pk_mul_f32 v[64:65], v[0:1], v[8:9]
	v_pk_mul_f32 v[66:67], v[2:3], v[10:11]
	v_pk_mul_f32 v[8:9], v[40:41], v[12:13] op_sel_hi:[1,0]
	v_pk_mul_f32 v[10:11], v[38:39], v[12:13] op_sel_hi:[1,0]
	v_pk_mul_f32 v[150:151], v[6:7], v[150:151]
	v_pk_mul_f32 v[148:149], v[4:5], v[148:149]
	v_pk_mul_f32 v[118:119], v[6:7], v[118:119]
	v_pk_mul_f32 v[120:121], v[4:5], v[120:121]
	v_pk_mul_f32 v[38:39], v[6:7], v[10:11]
	v_pk_mul_f32 v[40:41], v[4:5], v[8:9]
	v_pk_mul_f32 v[4:5], v[42:43], v[12:13] op_sel_hi:[1,0]
	v_pk_mul_f32 v[6:7], v[36:37], v[12:13] op_sel_hi:[1,0]
	v_pk_mul_f32 v[152:153], v[0:1], v[30:31]
	v_pk_mul_f32 v[180:181], v[0:1], v[176:177]
	v_pk_mul_f32 v[144:145], v[0:1], v[144:145]
	v_pk_mul_f32 v[122:123], v[0:1], v[122:123]
	v_pk_mul_f32 v[58:59], v[0:1], v[22:23]
	v_pk_mul_f32 v[36:37], v[2:3], v[6:7]
	v_pk_mul_f32 v[42:43], v[0:1], v[4:5]
